# GEMM phases: static s_setprio 1 for waves 0-3 instead of 4-7
# baseline (speedup 1.0000x reference)
; __device__ __forceinline__ int lt_tid(int wv) { int ln; asm volatile("v_mbcnt_lo_u32_b32 %0, -1, 0\n\tv_mbcnt_hi_u32_b32 %0, -1, %0" : "=v"(ln)); return (wv << 6) | ln; }
;     __device__ __forceinline__ const char* b_ptr(const Unit& u) const { return (const char*)Bt + ((size_t)u.pn * BM * K + u.koff) * 2; }
;     __device__ __forceinline__ const char* b_ptr(const Unit& u) const { return (const char*)Bt + ((size_t)u.e * bstride + (size_t)u.pn * BM * K) * 2; }
; #define PG8_STAGE(bufoff, gbase, voff) do { _Pragma("unroll") for (int _i = 0; _i < 2; ++_i) \
;         __builtin_amdgcn_global_load_lds((const unsigned*)((const char*)(gbase) + (voff)[_i]), (LAS unsigned*)(lds + (bufoff) + ldsw + _i * 8192), 16, 0, 0); } while (0)
; #define PG8_BAR __builtin_amdgcn_s_barrier()
; template <class Epi, class Sched>
; __device__ __forceinline__ void gemm_phase(LAS unsigned char* lds, const bf16_t* Abase, const int K, const Sched& S, const Epi& E, const int wvid) {
;     const int tid = lt_tid(wvid), wid = __builtin_amdgcn_readfirstlane(tid >> 6), lane = tid & 63, wr = wid >> 2, wc = wid & 3, fr = lane & 15, fq = lane >> 4;
;     unsigned voffB[2];
; #pragma unroll
;     for (int i = 0; i < 2; ++i) { int R, C; stage_rc(tid * 16 + i * 8192, R, C); const int Rb = Epi::PERM ? ((R & ~31) + perm32(R & 31)) : R;
;         voffB[i] = (unsigned)(Rb * K + C) * 2u; }
;     const size_t kstep = (size_t)(BK * 2);
;     const size_t hstep = (size_t)HALF * K * 2;
;     const unsigned ldsw = (unsigned)wid * 1024u;
;     const int aoff = lds_byte(wr * 64 + fr, fq * 8), boff = lds_byte(wc * 32 + fr, fq * 8);
;     ...
;     Unit cur, nxt; int ui = 0;
;     if (!S.next(0, cur)) return;
;     f32x4 acc[2][2][4][2];
; #pragma unroll
;     for (int a = 0; a < 2; ++a)
; #pragma unroll
;         for (int b = 0; b < 2; ++b)
; #pragma unroll
;             for (int m = 0; m < 4; ++m)
; #pragma unroll
;                 for (int n = 0; n < 2; ++n) acc[a][b][m][n] = (f32x4){0.f, 0.f, 0.f, 0.f};
;     bf16x8 At[4][2], B0[2][2], B1[2][2];
;     unsigned voffA[2][2];
;     PG8_AOFF(cur);
;     const char* Ab = (const char*)Abase;
;     const char* cB = S.b_ptr(cur);
;     PG8_STAGE(PG8_SB(0, 0), cB, voffB); PG8_STAGE(PG8_SA(0, 0), Ab, voffA[0]); PG8_STAGE(PG8_SB(0, 1), cB + hstep, voffB); PG8_STAGE(PG8_SA(0, 1), Ab, voffA[1]);
;     if (wr == 1) PG8_BAR;
.LBB0_113:
	v_readlane_b32 s2, v254, 52
	v_readlane_b32 s3, v254, 53
	s_xor_b64 s[2:3], s[2:3], -1
	v_writelane_b32 v255, s2, 10
	s_add_u32 s6, s8, 0x13270000
	s_addc_u32 s7, s9, 0
	v_writelane_b32 v255, s3, 11
	s_andn2_b64 vcc, exec, s[0:1]
	s_cbranch_vccnz .LBB0_205
	v_ashrrev_i32_e32 v3, 31, v0
	v_lshrrev_b32_e32 v3, 26, v3
	v_lshlrev_b32_e32 v2, 4, v0
	v_add_u32_e32 v3, v0, v3
	v_bfe_i32 v0, v0, 27, 1
	v_lshrrev_b32_e32 v0, 22, v0
	v_add_u32_e32 v0, v2, v0
	v_and_b32_e32 v0, 0xfffffc00, v0
	v_sub_u32_e32 v0, v2, v0
	v_lshrrev_b32_e32 v4, 4, v0
	v_bitop3_b32 v0, v4, v0, 32 bitop3:0x6c
	v_ashrrev_i32_e32 v5, 31, v0
	v_readlane_b32 s0, v254, 49
	v_ashrrev_i32_e32 v3, 6, v3
	v_lshrrev_b32_e32 v5, 26, v5
	s_mul_i32 s40, s0, 0x2c0000
	v_lshlrev_b32_e32 v4, 3, v3
	v_add_u32_e32 v5, v0, v5
	s_lshl_b64 s[0:1], s[40:41], 1
	v_and_b32_e32 v4, -16, v4
	v_ashrrev_i32_e32 v7, 6, v5
	v_and_b32_e32 v5, 0xc0, v5
	s_add_u32 s38, s6, s0
	v_add_u32_e32 v4, v7, v4
	v_sub_u32_e32 v0, v0, v5
	s_addc_u32 s39, s7, s1
	v_lshlrev_b32_e32 v3, 5, v3
	v_ashrrev_i16_sdwa v0, v216, sext(v0) dst_sel:DWORD dst_unused:UNUSED_PAD src0_sel:DWORD src1_sel:BYTE_0
	v_lshlrev_b32_e32 v5, 1, v4
	s_waitcnt vmcnt(5)
	v_lshrrev_b32_e32 v8, 2, v4
	v_and_b32_e32 v7, 3, v7
	s_mov_b32 s1, 0x1fffe0
	v_and_b32_e32 v3, 32, v3
	v_bfe_i32 v0, v0, 0, 16
	v_and_b32_e32 v5, 24, v5
	v_and_b32_e32 v8, 4, v8
	v_and_or_b32 v4, v4, s1, v7
	v_or3_b32 v4, v4, v8, v5
	v_add_lshl_u32 v0, v3, v0, 1
	v_lshl_add_u32 v178, v4, 11, v0
	v_add_u32_e32 v0, 0x2000, v2
	v_ashrrev_i32_e32 v2, 31, v0
	v_lshrrev_b32_e32 v2, 22, v2
	v_add_u32_e32 v2, v0, v2
	v_ashrrev_i32_e32 v2, 10, v2
	v_mul_i32_i24_e32 v3, 0x400, v2
	v_sub_u32_e32 v0, v0, v3
	v_lshrrev_b32_e32 v3, 4, v0
	v_bitop3_b32 v0, v3, v0, 32 bitop3:0x6c
	v_ashrrev_i32_e32 v4, 31, v0
	v_lshrrev_b32_e32 v4, 26, v4
	v_lshlrev_b32_e32 v3, 3, v2
	v_add_u32_e32 v4, v0, v4
	v_and_b32_e32 v3, -16, v3
	v_ashrrev_i32_e32 v5, 6, v4
	v_and_b32_e32 v4, 0xc0, v4
	v_add_u32_e32 v3, v5, v3
	v_sub_u32_e32 v0, v0, v4
	v_lshlrev_b32_e32 v2, 5, v2
	v_ashrrev_i16_sdwa v0, v216, sext(v0) dst_sel:DWORD dst_unused:UNUSED_PAD src0_sel:DWORD src1_sel:BYTE_0
	v_lshlrev_b32_e32 v4, 1, v3
	v_lshrrev_b32_e32 v7, 2, v3
	v_and_b32_e32 v5, 3, v5
	v_and_b32_e32 v2, 32, v2
	v_bfe_i32 v0, v0, 0, 16
	v_and_b32_e32 v4, 24, v4
	v_and_b32_e32 v7, 4, v7
	v_and_or_b32 v3, v3, s1, v5
	v_or3_b32 v3, v3, v7, v4
	v_add_lshl_u32 v0, v2, v0, 1
	v_lshl_add_u32 v180, v3, 11, v0
	v_mbcnt_lo_u32_b32 v0, -1, 0
	v_mbcnt_hi_u32_b32 v0, -1, v0
	s_add_u32 s10, s8, 0x10000
	v_or_b32_e32 v0, s75, v0
	v_ashrrev_i32_e32 v3, 31, v0
	v_lshrrev_b32_e32 v3, 26, v3
	v_lshlrev_b32_e32 v2, 4, v0
	v_add_u32_e32 v3, v0, v3
	v_bfe_i32 v0, v0, 27, 1
	v_lshrrev_b32_e32 v0, 22, v0
	v_add_u32_e32 v0, v2, v0
	v_and_b32_e32 v0, 0xfffffc00, v0
	v_sub_u32_e32 v0, v2, v0
	v_lshrrev_b32_e32 v4, 4, v0
	v_bitop3_b32 v0, v4, v0, 32 bitop3:0x6c
	v_ashrrev_i32_e32 v5, 31, v0
	v_lshrrev_b32_e32 v5, 26, v5
	v_ashrrev_i32_e32 v3, 6, v3
	v_add_u32_e32 v5, v0, v5
	v_lshlrev_b32_e32 v4, 3, v3
	v_lshrrev_b32_e32 v7, 6, v5
	v_and_b32_e32 v5, 0xc0, v5
	v_and_b32_e32 v4, 0x1ffff0, v4
	v_lshlrev_b32_e32 v3, 5, v3
	v_sub_u32_e32 v0, v0, v5
	v_and_b32_e32 v3, 32, v3
	v_ashrrev_i16_sdwa v0, v216, sext(v0) dst_sel:DWORD dst_unused:UNUSED_PAD src0_sel:DWORD src1_sel:BYTE_0
	v_add_u32_e32 v4, s57, v4
	v_add_u32_sdwa v0, v3, sext(v0) dst_sel:DWORD dst_unused:UNUSED_PAD src0_sel:DWORD src1_sel:WORD_0
	v_add_lshl_u32 v3, v4, v7, 11
	v_add_u32_e32 v2, 0x2000, v2
	v_lshl_add_u32 v0, v0, 1, v3
	v_ashrrev_i32_e32 v3, 31, v2
	v_lshrrev_b32_e32 v3, 22, v3
	v_add_u32_e32 v3, v2, v3
	v_ashrrev_i32_e32 v3, 10, v3
	v_mul_i32_i24_e32 v4, 0x400, v3
	v_sub_u32_e32 v2, v2, v4
	v_lshrrev_b32_e32 v4, 4, v2
	s_addc_u32 s11, s9, 0
	s_ashr_i32 s1, s37, 6
	v_bitop3_b32 v2, v4, v2, 32 bitop3:0x6c
	s_ashr_i32 s17, s16, 31
	s_ashr_i32 s0, s37, 8
	s_lshl_b32 s40, s1, 10
	v_ashrrev_i32_e32 v5, 31, v2
	s_lshl_b64 s[2:3], s[16:17], 19
	v_lshrrev_b32_e32 v5, 26, v5
	s_add_u32 s4, s38, s2
	v_add_u32_e32 v5, v2, v5
	s_addc_u32 s5, s39, s3
	s_add_i32 s17, s40, 0
	v_lshlrev_b32_e32 v4, 3, v3
	v_lshrrev_b32_e32 v7, 6, v5
	v_and_b32_e32 v5, 0xc0, v5
	s_add_i32 s42, s17, 0x10000
	v_and_b32_e32 v4, 0x1ffff0, v4
	v_lshlrev_b32_e32 v3, 5, v3
	v_sub_u32_e32 v2, v2, v5
	s_mov_b32 m0, s42
	s_add_i32 s43, s17, 0x12000
	v_and_b32_e32 v3, 32, v3
	v_ashrrev_i16_sdwa v2, v216, sext(v2) dst_sel:DWORD dst_unused:UNUSED_PAD src0_sel:DWORD src1_sel:BYTE_0
	v_add_u32_e32 v4, s57, v4
	global_load_lds_dwordx4 v178, s[4:5]
	s_mov_b32 m0, s43
	v_add_u32_sdwa v2, v3, sext(v2) dst_sel:DWORD dst_unused:UNUSED_PAD src0_sel:DWORD src1_sel:WORD_0
	v_add_lshl_u32 v3, v4, v7, 11
	global_load_lds_dwordx4 v180, s[4:5]
	s_mov_b32 m0, s17
	s_add_i32 s46, s17, 0x2000
	v_lshl_add_u32 v184, v2, 1, v3
	global_load_lds_dwordx4 v0, s[10:11]
	s_mov_b32 m0, s46
	s_add_u32 s2, s4, 0x40000
	global_load_lds_dwordx4 v184, s[10:11]
	s_addc_u32 s3, s5, 0
	s_add_i32 m0, s17, 0x14000
	s_add_i32 s47, s17, 0x4000
	global_load_lds_dwordx4 v178, s[2:3]
	s_add_i32 m0, s17, 0x16000
	v_add_u32_e32 v182, 0x40000, v0
	global_load_lds_dwordx4 v180, s[2:3]
	s_mov_b32 m0, s47
	s_add_i32 s48, s17, 0x6000
	v_add_u32_e32 v186, 0x40000, v184
	global_load_lds_dwordx4 v182, s[10:11]
	s_mov_b32 m0, s48
	v_mov_b32_e32 v179, v1
	global_load_lds_dwordx4 v186, s[10:11]
	v_mov_b32_e32 v181, v1
	v_lshl_add_u64 v[2:3], s[4:5], 0, v[178:179]
	s_setprio 1
	s_cmp_lg_u32 s0, 1
	v_lshl_add_u64 v[4:5], s[4:5], 0, v[180:181]
	s_cbranch_scc1 .LBB0_116
	s_barrier
	s_setprio 0

; __device__ __forceinline__ int lt_tid(int wv) { int ln; asm volatile("v_mbcnt_lo_u32_b32 %0, -1, 0\n\tv_mbcnt_hi_u32_b32 %0, -1, %0" : "=v"(ln)); return (wv << 6) | ln; }
;     __device__ __forceinline__ const char* b_ptr(const Unit& u) const { return (const char*)Bt + ((size_t)u.pn * BM * K + u.koff) * 2; }
;     __device__ __forceinline__ const char* b_ptr(const Unit& u) const { return (const char*)Bt + ((size_t)u.e * bstride + (size_t)u.pn * BM * K) * 2; }
; #define PG8_STAGE(bufoff, gbase, voff) do { _Pragma("unroll") for (int _i = 0; _i < 2; ++_i) \
;         __builtin_amdgcn_global_load_lds((const unsigned*)((const char*)(gbase) + (voff)[_i]), (LAS unsigned*)(lds + (bufoff) + ldsw + _i * 8192), 16, 0, 0); } while (0)
; #define PG8_BAR __builtin_amdgcn_s_barrier()
; template <class Epi, class Sched>
; __device__ __forceinline__ void gemm_phase(LAS unsigned char* lds, const bf16_t* Abase, const int K, const Sched& S, const Epi& E, const int wvid) {
;     const int tid = lt_tid(wvid), wid = __builtin_amdgcn_readfirstlane(tid >> 6), lane = tid & 63, wr = wid >> 2, wc = wid & 3, fr = lane & 15, fq = lane >> 4;
;     unsigned voffB[2];
; #pragma unroll
;     for (int i = 0; i < 2; ++i) { int R, C; stage_rc(tid * 16 + i * 8192, R, C); const int Rb = Epi::PERM ? ((R & ~31) + perm32(R & 31)) : R;
;         voffB[i] = (unsigned)(Rb * K + C) * 2u; }
;     const size_t kstep = (size_t)(BK * 2);
;     const size_t hstep = (size_t)HALF * K * 2;
;     const unsigned ldsw = (unsigned)wid * 1024u;
;     const int aoff = lds_byte(wr * 64 + fr, fq * 8), boff = lds_byte(wc * 32 + fr, fq * 8);
;     ...
;     Unit cur, nxt; int ui = 0;
;     if (!S.next(0, cur)) return;
;     f32x4 acc[2][2][4][2];
; #pragma unroll
;     for (int a = 0; a < 2; ++a)
; #pragma unroll
;         for (int b = 0; b < 2; ++b)
; #pragma unroll
;             for (int m = 0; m < 4; ++m)
; #pragma unroll
;                 for (int n = 0; n < 2; ++n) acc[a][b][m][n] = (f32x4){0.f, 0.f, 0.f, 0.f};
;     bf16x8 At[4][2], B0[2][2], B1[2][2];
;     unsigned voffA[2][2];
;     PG8_AOFF(cur);
;     const char* Ab = (const char*)Abase;
;     const char* cB = S.b_ptr(cur);
;     PG8_STAGE(PG8_SB(0, 0), cB, voffB); PG8_STAGE(PG8_SA(0, 0), Ab, voffA[0]); PG8_STAGE(PG8_SB(0, 1), cB + hstep, voffB); PG8_STAGE(PG8_SA(0, 1), Ab, voffA[1]);
;     if (wr == 1) PG8_BAR;
.LBB0_984:
	v_ashrrev_i32_e32 v3, 31, v0
	v_lshrrev_b32_e32 v3, 26, v3
	v_lshlrev_b32_e32 v2, 4, v0
	v_add_u32_e32 v3, v0, v3
	v_bfe_i32 v0, v0, 27, 1
	v_lshrrev_b32_e32 v0, 22, v0
	v_add_u32_e32 v0, v2, v0
	v_and_b32_e32 v0, 0xfffffc00, v0
	v_sub_u32_e32 v0, v2, v0
	v_lshrrev_b32_e32 v4, 4, v0
	v_bitop3_b32 v0, v4, v0, 32 bitop3:0x6c
	v_ashrrev_i32_e32 v5, 31, v0
	v_ashrrev_i32_e32 v3, 6, v3
	v_lshrrev_b32_e32 v5, 26, v5
	v_lshlrev_b32_e32 v4, 3, v3
	v_add_u32_e32 v5, v0, v5
	v_and_b32_e32 v4, -16, v4
	v_ashrrev_i32_e32 v7, 6, v5
	v_and_b32_e32 v5, 0xc0, v5
	v_add_u32_e32 v4, v7, v4
	v_sub_u32_e32 v0, v0, v5
	v_lshlrev_b32_e32 v3, 5, v3
	v_ashrrev_i16_sdwa v0, v216, sext(v0) dst_sel:DWORD dst_unused:UNUSED_PAD src0_sel:DWORD src1_sel:BYTE_0
	v_lshlrev_b32_e32 v5, 1, v4
	v_lshrrev_b32_e32 v8, 2, v4
	v_and_b32_e32 v7, 3, v7
	s_mov_b32 s5, 0x1fffe0
	v_and_b32_e32 v3, 32, v3
	v_bfe_i32 v0, v0, 0, 16
	v_and_b32_e32 v5, 24, v5
	v_and_b32_e32 v8, 4, v8
	v_and_or_b32 v4, v4, s5, v7
	v_or3_b32 v4, v4, v8, v5
	v_add_lshl_u32 v0, v3, v0, 1
	v_lshl_add_u32 v178, v4, 11, v0
	v_add_u32_e32 v0, 0x2000, v2
	v_ashrrev_i32_e32 v2, 31, v0
	v_lshrrev_b32_e32 v2, 22, v2
	v_add_u32_e32 v2, v0, v2
	v_ashrrev_i32_e32 v2, 10, v2
	v_mul_i32_i24_e32 v3, 0x400, v2
	v_sub_u32_e32 v0, v0, v3
	v_lshrrev_b32_e32 v3, 4, v0
	v_bitop3_b32 v0, v3, v0, 32 bitop3:0x6c
	v_ashrrev_i32_e32 v4, 31, v0
	v_lshrrev_b32_e32 v4, 26, v4
	v_lshlrev_b32_e32 v3, 3, v2
	v_add_u32_e32 v4, v0, v4
	v_and_b32_e32 v3, -16, v3
	v_ashrrev_i32_e32 v5, 6, v4
	v_and_b32_e32 v4, 0xc0, v4
	v_add_u32_e32 v3, v5, v3
	v_sub_u32_e32 v0, v0, v4
	v_lshlrev_b32_e32 v2, 5, v2
	v_ashrrev_i16_sdwa v0, v216, sext(v0) dst_sel:DWORD dst_unused:UNUSED_PAD src0_sel:DWORD src1_sel:BYTE_0
	v_lshlrev_b32_e32 v4, 1, v3
	v_lshrrev_b32_e32 v7, 2, v3
	v_and_b32_e32 v5, 3, v5
	v_and_b32_e32 v2, 32, v2
	v_bfe_i32 v0, v0, 0, 16
	v_and_b32_e32 v4, 24, v4
	v_and_b32_e32 v7, 4, v7
	v_and_or_b32 v3, v3, s5, v5
	v_or3_b32 v3, v3, v7, v4
	v_add_lshl_u32 v0, v2, v0, 1
	v_lshl_add_u32 v180, v3, 11, v0
	v_mbcnt_lo_u32_b32 v0, -1, 0
	v_mbcnt_hi_u32_b32 v0, -1, v0
	s_ashr_i32 s0, s6, 31
	v_or_b32_e32 v0, s75, v0
	v_ashrrev_i32_e32 v3, 31, v0
	v_lshrrev_b32_e32 v3, 26, v3
	s_lshr_b32 s0, s0, 30
	v_lshlrev_b32_e32 v2, 4, v0
	v_add_u32_e32 v3, v0, v3
	v_bfe_i32 v0, v0, 27, 1
	s_add_i32 s6, s6, s0
	v_readlane_b32 s0, v254, 49
	v_lshrrev_b32_e32 v0, 22, v0
	s_ashr_i32 s4, s6, 2
	s_lshl_b32 s0, s0, 21
	v_add_u32_e32 v0, v2, v0
	s_add_u32 s0, s10, s0
	v_and_b32_e32 v0, 0xfffffc00, v0
	s_addc_u32 s1, s11, 0
	v_sub_u32_e32 v0, v2, v0
	s_add_u32 s38, s0, 0x13d70000
	v_lshrrev_b32_e32 v4, 4, v0
	s_addc_u32 s39, s1, 0
	v_bitop3_b32 v0, v4, v0, 32 bitop3:0x6c
	s_add_u32 s0, s10, 0xf1f0000
	v_ashrrev_i32_e32 v5, 31, v0
	s_addc_u32 s1, s11, 0
	s_ashr_i32 s7, s37, 6
	v_lshrrev_b32_e32 v5, 26, v5
	s_ashr_i32 s6, s37, 8
	s_lshl_b32 s40, s7, 10
	s_lshl_b32 s5, s4, 8
	v_ashrrev_i32_e32 v3, 6, v3
	v_add_u32_e32 v5, v0, v5
	s_and_b64 s[16:17], exec, s[2:3]
	v_lshlrev_b32_e32 v4, 3, v3
	v_lshrrev_b32_e32 v7, 6, v5
	v_and_b32_e32 v5, 0xc0, v5
	s_cselect_b32 s16, 0, s5
	v_and_b32_e32 v4, 0x1ffff0, v4
	v_lshlrev_b32_e32 v3, 5, v3
	v_sub_u32_e32 v0, v0, v5
	v_ashrrev_i16_sdwa v0, v216, sext(v0) dst_sel:DWORD dst_unused:UNUSED_PAD src0_sel:DWORD src1_sel:BYTE_0
	v_add_u32_e32 v4, s9, v4
	v_and_or_b32 v3, v3, 32, s16
	v_add_u32_sdwa v0, v3, sext(v0) dst_sel:DWORD dst_unused:UNUSED_PAD src0_sel:DWORD src1_sel:WORD_0
	v_add_lshl_u32 v3, v4, v7, 11
	v_add_u32_e32 v2, 0x2000, v2
	v_lshl_add_u32 v0, v0, 1, v3
	v_ashrrev_i32_e32 v3, 31, v2
	v_lshrrev_b32_e32 v3, 22, v3
	v_add_u32_e32 v3, v2, v3
	v_ashrrev_i32_e32 v3, 10, v3
	v_mul_i32_i24_e32 v4, 0x400, v3
	v_sub_u32_e32 v2, v2, v4
	v_lshrrev_b32_e32 v4, 4, v2
	v_bitop3_b32 v2, v4, v2, 32 bitop3:0x6c
	v_lshlrev_b32_e32 v4, 3, v3
	v_lshlrev_b32_e32 v3, 5, v3
	s_ashr_i32 s23, s22, 31
	s_ashr_i32 s17, s16, 31
	v_and_or_b32 v3, v3, 32, s16
	s_lshl_b64 s[18:19], s[22:23], 19
	s_lshl_b64 s[16:17], s[16:17], 1
	s_add_u32 s5, s38, s18
	v_ashrrev_i32_e32 v5, 31, v2
	s_addc_u32 s8, s39, s19
	v_lshrrev_b32_e32 v5, 26, v5
	s_add_u32 s26, s5, s16
	v_add_u32_e32 v5, v2, v5
	s_addc_u32 s27, s8, s17
	s_add_i32 s42, s40, 0
	v_lshrrev_b32_e32 v7, 6, v5
	v_and_b32_e32 v5, 0xc0, v5
	s_add_i32 s43, s42, 0x10000
	v_and_b32_e32 v4, 0x1ffff0, v4
	v_sub_u32_e32 v2, v2, v5
	s_mov_b32 m0, s43
	s_add_i32 s46, s42, 0x12000
	v_ashrrev_i16_sdwa v2, v216, sext(v2) dst_sel:DWORD dst_unused:UNUSED_PAD src0_sel:DWORD src1_sel:BYTE_0
	v_add_u32_e32 v4, s9, v4
	global_load_lds_dwordx4 v178, s[26:27]
	s_mov_b32 m0, s46
	v_add_u32_sdwa v2, v3, sext(v2) dst_sel:DWORD dst_unused:UNUSED_PAD src0_sel:DWORD src1_sel:WORD_0
	v_add_lshl_u32 v3, v4, v7, 11
	global_load_lds_dwordx4 v180, s[26:27]
	s_mov_b32 m0, s42
	s_add_i32 s47, s42, 0x2000
	v_lshl_add_u32 v184, v2, 1, v3
	global_load_lds_dwordx4 v0, s[0:1]
	s_mov_b32 m0, s47
	s_add_u32 s16, s26, 0x40000
	global_load_lds_dwordx4 v184, s[0:1]
	s_addc_u32 s17, s27, 0
	s_add_i32 m0, s42, 0x14000
	s_add_i32 s48, s42, 0x4000
	global_load_lds_dwordx4 v178, s[16:17]
	s_add_i32 m0, s42, 0x16000
	v_add_u32_e32 v182, 0x40000, v0
	global_load_lds_dwordx4 v180, s[16:17]
	s_mov_b32 m0, s48
	s_add_i32 s49, s42, 0x6000
	v_add_u32_e32 v186, 0x40000, v184
	global_load_lds_dwordx4 v182, s[0:1]
	s_mov_b32 m0, s49
	v_mov_b32_e32 v179, v1
	global_load_lds_dwordx4 v186, s[0:1]
	v_mov_b32_e32 v181, v1
	v_lshl_add_u64 v[2:3], s[26:27], 0, v[178:179]
	s_setprio 1
	s_cmp_lg_u32 s6, 1
	v_lshl_add_u64 v[4:5], s[26:27], 0, v[180:181]
	s_cbranch_scc1 .LBB0_986
	s_barrier
	s_setprio 0

; __device__ __forceinline__ int lt_tid(int wv) { int ln; asm volatile("v_mbcnt_lo_u32_b32 %0, -1, 0\n\tv_mbcnt_hi_u32_b32 %0, -1, %0" : "=v"(ln)); return (wv << 6) | ln; }
;     __device__ __forceinline__ const char* b_ptr(const Unit& u) const { return (const char*)Bt + ((size_t)u.pn * BM * K + u.koff) * 2; }
;     __device__ __forceinline__ const char* b_ptr(const Unit& u) const { return (const char*)Bt + ((size_t)u.e * bstride + (size_t)u.pn * BM * K) * 2; }
; #define PG8_STAGE(bufoff, gbase, voff) do { _Pragma("unroll") for (int _i = 0; _i < 2; ++_i) \
;         __builtin_amdgcn_global_load_lds((const unsigned*)((const char*)(gbase) + (voff)[_i]), (LAS unsigned*)(lds + (bufoff) + ldsw + _i * 8192), 16, 0, 0); } while (0)
; #define PG8_BAR __builtin_amdgcn_s_barrier()
; template <class Epi, class Sched>
; __device__ __forceinline__ void gemm_phase(LAS unsigned char* lds, const bf16_t* Abase, const int K, const Sched& S, const Epi& E, const int wvid) {
;     const int tid = lt_tid(wvid), wid = __builtin_amdgcn_readfirstlane(tid >> 6), lane = tid & 63, wr = wid >> 2, wc = wid & 3, fr = lane & 15, fq = lane >> 4;
;     unsigned voffB[2];
; #pragma unroll
;     for (int i = 0; i < 2; ++i) { int R, C; stage_rc(tid * 16 + i * 8192, R, C); const int Rb = Epi::PERM ? ((R & ~31) + perm32(R & 31)) : R;
;         voffB[i] = (unsigned)(Rb * K + C) * 2u; }
;     const size_t kstep = (size_t)(BK * 2);
;     const size_t hstep = (size_t)HALF * K * 2;
;     const unsigned ldsw = (unsigned)wid * 1024u;
;     const int aoff = lds_byte(wr * 64 + fr, fq * 8), boff = lds_byte(wc * 32 + fr, fq * 8);
;     ...
;     Unit cur, nxt; int ui = 0;
;     if (!S.next(0, cur)) return;
;     f32x4 acc[2][2][4][2];
; #pragma unroll
;     for (int a = 0; a < 2; ++a)
; #pragma unroll
;         for (int b = 0; b < 2; ++b)
; #pragma unroll
;             for (int m = 0; m < 4; ++m)
; #pragma unroll
;                 for (int n = 0; n < 2; ++n) acc[a][b][m][n] = (f32x4){0.f, 0.f, 0.f, 0.f};
;     bf16x8 At[4][2], B0[2][2], B1[2][2];
;     unsigned voffA[2][2];
;     PG8_AOFF(cur);
;     const char* Ab = (const char*)Abase;
;     const char* cB = S.b_ptr(cur);
;     PG8_STAGE(PG8_SB(0, 0), cB, voffB); PG8_STAGE(PG8_SA(0, 0), Ab, voffA[0]); PG8_STAGE(PG8_SB(0, 1), cB + hstep, voffB); PG8_STAGE(PG8_SA(0, 1), Ab, voffA[1]);
;     if (wr == 1) PG8_BAR;
.LBB0_1198:
	v_ashrrev_i32_e32 v7, 31, v6
	v_lshrrev_b32_e32 v7, 26, v7
	v_lshlrev_b32_e32 v0, 4, v6
	v_add_u32_e32 v7, v6, v7
	v_bfe_i32 v6, v6, 27, 1
	v_lshrrev_b32_e32 v6, 22, v6
	v_add_u32_e32 v6, v0, v6
	v_and_b32_e32 v6, 0xfffffc00, v6
	v_sub_u32_e32 v6, v0, v6
	v_lshrrev_b32_e32 v8, 4, v6
	v_bitop3_b32 v6, v8, v6, 32 bitop3:0x6c
	v_ashrrev_i32_e32 v9, 31, v6
	v_ashrrev_i32_e32 v7, 6, v7
	v_lshrrev_b32_e32 v9, 26, v9
	v_lshlrev_b32_e32 v8, 3, v7
	v_add_u32_e32 v9, v6, v9
	v_and_b32_e32 v8, -16, v8
	v_ashrrev_i32_e32 v10, 6, v9
	v_and_b32_e32 v9, 0xc0, v9
	v_add_u32_e32 v8, v10, v8
	v_sub_u32_e32 v6, v6, v9
	v_lshlrev_b32_e32 v7, 5, v7
	v_ashrrev_i16_sdwa v6, v216, sext(v6) dst_sel:DWORD dst_unused:UNUSED_PAD src0_sel:DWORD src1_sel:BYTE_0
	v_lshlrev_b32_e32 v9, 1, v8
	v_lshrrev_b32_e32 v11, 2, v8
	v_and_b32_e32 v10, 3, v10
	s_mov_b32 s1, 0x1fffe0
	v_and_b32_e32 v7, 32, v7
	v_bfe_i32 v6, v6, 0, 16
	v_and_b32_e32 v9, 24, v9
	v_and_b32_e32 v11, 4, v11
	v_and_or_b32 v8, v8, s1, v10
	v_or3_b32 v8, v8, v11, v9
	v_add_lshl_u32 v6, v7, v6, 1
	v_add_u32_e32 v0, 0x2000, v0
	v_lshl_add_u32 v180, v8, 11, v6
	v_ashrrev_i32_e32 v6, 31, v0
	v_lshrrev_b32_e32 v6, 22, v6
	v_add_u32_e32 v6, v0, v6
	v_ashrrev_i32_e32 v6, 10, v6
	v_mul_i32_i24_e32 v7, 0x400, v6
	v_sub_u32_e32 v0, v0, v7
	v_lshrrev_b32_e32 v7, 4, v0
	v_bitop3_b32 v0, v7, v0, 32 bitop3:0x6c
	v_ashrrev_i32_e32 v8, 31, v0
	v_lshrrev_b32_e32 v8, 26, v8
	v_lshlrev_b32_e32 v7, 3, v6
	v_add_u32_e32 v8, v0, v8
	v_and_b32_e32 v7, -16, v7
	v_ashrrev_i32_e32 v9, 6, v8
	v_and_b32_e32 v8, 0xc0, v8
	v_add_u32_e32 v7, v9, v7
	v_sub_u32_e32 v0, v0, v8
	v_lshlrev_b32_e32 v6, 5, v6
	v_ashrrev_i16_sdwa v0, v216, sext(v0) dst_sel:DWORD dst_unused:UNUSED_PAD src0_sel:DWORD src1_sel:BYTE_0
	v_lshlrev_b32_e32 v8, 1, v7
	v_lshrrev_b32_e32 v10, 2, v7
	v_and_b32_e32 v9, 3, v9
	v_and_b32_e32 v6, 32, v6
	v_bfe_i32 v0, v0, 0, 16
	v_and_b32_e32 v8, 24, v8
	v_and_b32_e32 v10, 4, v10
	v_and_or_b32 v7, v7, s1, v9
	v_or3_b32 v7, v7, v10, v8
	v_add_lshl_u32 v0, v6, v0, 1
	v_lshl_add_u32 v182, v7, 11, v0
	v_mbcnt_lo_u32_b32 v0, -1, 0
	v_mbcnt_hi_u32_b32 v0, -1, v0
	v_readlane_b32 s0, v254, 49
	v_or_b32_e32 v0, s75, v0
	v_ashrrev_i32_e32 v6, 31, v0
	v_lshrrev_b32_e32 v6, 26, v6
	v_lshlrev_b32_e32 v8, 4, v0
	v_add_u32_e32 v6, v0, v6
	v_bfe_i32 v0, v0, 27, 1
	v_lshrrev_b32_e32 v0, 22, v0
	v_add_u32_e32 v0, v8, v0
	v_and_b32_e32 v0, 0xfffffc00, v0
	v_sub_u32_e32 v0, v8, v0
	v_lshrrev_b32_e32 v7, 4, v0
	v_bitop3_b32 v0, v7, v0, 32 bitop3:0x6c
	v_ashrrev_i32_e32 v10, 31, v0
	v_ashrrev_i32_e32 v6, 6, v6
	v_lshrrev_b32_e32 v10, 26, v10
	v_lshlrev_b32_e32 v7, 3, v6
	v_add_u32_e32 v10, v0, v10
	v_and_b32_e32 v7, -16, v7
	v_ashrrev_i32_e32 v11, 6, v10
	v_add_u32_e32 v11, v11, v7
	v_and_b32_e32 v7, 0xc0, v10
	v_sub_u32_e32 v0, v0, v7
	v_lshlrev_b32_e32 v6, 5, v6
	v_ashrrev_i16_sdwa v0, v216, sext(v0) dst_sel:DWORD dst_unused:UNUSED_PAD src0_sel:DWORD src1_sel:BYTE_0
	s_lshl_b32 s0, s0, 25
	v_and_b32_e32 v6, 32, v6
	v_bfe_i32 v0, v0, 0, 16
	s_add_u32 s36, s6, s0
	v_add_u32_e32 v9, -1, v179
	v_add_lshl_u32 v10, v6, v0, 1
	v_add_u32_e32 v0, v11, v228
	s_addc_u32 s37, s7, 0
	v_min_i32_e32 v0, v0, v9
	s_add_u32 s10, s8, 0x1a230c00
	v_add_u32_e32 v6, v0, v5
	s_addc_u32 s11, s9, 0
	v_ashrrev_i32_e32 v7, 31, v6
	v_lshl_add_u64 v[6:7], v[6:7], 2, s[10:11]
	v_add_u32_e32 v12, 0x80, v228
	global_load_dword v0, v[6:7], off
	v_add_u32_e32 v6, v11, v12
	v_min_i32_e32 v6, v6, v9
	v_add_u32_e32 v6, v6, v5
	v_ashrrev_i32_e32 v7, 31, v6
	v_lshl_add_u64 v[6:7], v[6:7], 2, s[10:11]
	global_load_dword v6, v[6:7], off
	s_add_u32 s16, s8, 0x10000
	s_addc_u32 s17, s9, 0
	s_ashr_i32 s1, s35, 6
	s_ashr_i32 s25, s24, 31
	s_ashr_i32 s0, s35, 8
	s_lshl_b32 s38, s1, 10
	s_lshl_b64 s[2:3], s[24:25], 19
	s_add_u32 s2, s36, s2
	s_addc_u32 s3, s37, s3
	s_add_i32 s25, s38, 0
	v_lshl_add_u64 v[2:3], s[2:3], 0, v[2:3]
	s_add_i32 s39, s25, 0x10000
	s_mov_b32 m0, s39
	v_readfirstlane_b32 s2, v2
	v_readfirstlane_b32 s3, v3
	s_add_i32 s42, s25, 0x12000
	s_add_i32 s43, s25, 0x2000
	s_add_i32 s46, s25, 0x4000
	s_add_i32 s47, s25, 0x6000
	s_waitcnt vmcnt(1)
	v_lshl_add_u32 v0, v0, 11, v10
	global_load_lds_dwordx4 v180, s[2:3]
	s_mov_b32 m0, s42
	s_waitcnt vmcnt(0)
	v_lshl_add_u32 v186, v6, 11, v10
	v_add_u32_e32 v6, 0x2000, v8
	v_ashrrev_i32_e32 v7, 31, v6
	v_lshrrev_b32_e32 v7, 22, v7
	v_add_u32_e32 v7, v6, v7
	v_ashrrev_i32_e32 v7, 10, v7
	v_mul_i32_i24_e32 v8, 0x400, v7
	v_sub_u32_e32 v6, v6, v8
	v_lshrrev_b32_e32 v8, 4, v6
	v_bitop3_b32 v6, v8, v6, 32 bitop3:0x6c
	v_ashrrev_i32_e32 v10, 31, v6
	v_lshrrev_b32_e32 v10, 26, v10
	v_add_u32_e32 v10, v6, v10
	v_ashrrev_i32_e32 v11, 6, v10
	v_and_b32_e32 v10, 0xc0, v10
	v_lshlrev_b32_e32 v8, 3, v7
	v_sub_u32_e32 v6, v6, v10
	v_and_b32_e32 v8, -16, v8
	v_lshlrev_b32_e32 v7, 5, v7
	v_ashrrev_i16_sdwa v6, v216, sext(v6) dst_sel:DWORD dst_unused:UNUSED_PAD src0_sel:DWORD src1_sel:BYTE_0
	v_add_u32_e32 v8, v11, v8
	v_and_b32_e32 v7, 32, v7
	v_bfe_i32 v6, v6, 0, 16
	v_add_lshl_u32 v10, v7, v6, 1
	v_add_u32_e32 v6, v8, v228
	v_min_i32_e32 v6, v6, v9
	v_add_u32_e32 v6, v6, v5
	v_ashrrev_i32_e32 v7, 31, v6
	v_lshl_add_u64 v[6:7], v[6:7], 2, s[10:11]
	global_load_dword v6, v[6:7], off
	s_waitcnt vmcnt(0)
	v_lshl_add_u32 v184, v6, 11, v10
	v_add_u32_e32 v6, v8, v12
	v_min_i32_e32 v6, v6, v9
	v_add_u32_e32 v6, v6, v5
	v_ashrrev_i32_e32 v7, 31, v6
	v_lshl_add_u64 v[6:7], v[6:7], 2, s[10:11]
	global_load_dword v5, v[6:7], off
	v_lshl_add_u64 v[6:7], v[2:3], 0, s[90:91]
	global_load_lds_dwordx4 v182, s[2:3]
	s_mov_b32 m0, s25
	v_readfirstlane_b32 s2, v6
	global_load_lds_dwordx4 v0, s[16:17]
	s_mov_b32 m0, s43
	v_readfirstlane_b32 s3, v7
	global_load_lds_dwordx4 v184, s[16:17]
	s_add_i32 m0, s25, 0x14000
	s_waitcnt vmcnt(0)
	v_lshl_add_u32 v188, v5, 11, v10
	s_nop 0
	global_load_lds_dwordx4 v180, s[2:3]
	s_add_i32 m0, s25, 0x16000
	s_setprio 1
	s_cmp_lg_u32 s0, 1
	global_load_lds_dwordx4 v182, s[2:3]
	s_mov_b32 m0, s46
	s_nop 0
	global_load_lds_dwordx4 v186, s[16:17]
	s_mov_b32 m0, s47
	s_nop 0
	global_load_lds_dwordx4 v188, s[16:17]
	s_cbranch_scc1 .LBB0_1200
	s_barrier
	s_setprio 0

; __device__ __forceinline__ int lt_tid(int wv) { int ln; asm volatile("v_mbcnt_lo_u32_b32 %0, -1, 0\n\tv_mbcnt_hi_u32_b32 %0, -1, %0" : "=v"(ln)); return (wv << 6) | ln; }
;     __device__ __forceinline__ const char* b_ptr(const Unit& u) const { return (const char*)Bt + ((size_t)u.pn * BM * K + u.koff) * 2; }
;     __device__ __forceinline__ const char* b_ptr(const Unit& u) const { return (const char*)Bt + ((size_t)u.e * bstride + (size_t)u.pn * BM * K) * 2; }
; #define PG8_STAGE(bufoff, gbase, voff) do { _Pragma("unroll") for (int _i = 0; _i < 2; ++_i) \
;         __builtin_amdgcn_global_load_lds((const unsigned*)((const char*)(gbase) + (voff)[_i]), (LAS unsigned*)(lds + (bufoff) + ldsw + _i * 8192), 16, 0, 0); } while (0)
; #define PG8_BAR __builtin_amdgcn_s_barrier()
; template <class Epi, class Sched>
; __device__ __forceinline__ void gemm_phase(LAS unsigned char* lds, const bf16_t* Abase, const int K, const Sched& S, const Epi& E, const int wvid) {
;     const int tid = lt_tid(wvid), wid = __builtin_amdgcn_readfirstlane(tid >> 6), lane = tid & 63, wr = wid >> 2, wc = wid & 3, fr = lane & 15, fq = lane >> 4;
;     unsigned voffB[2];
; #pragma unroll
;     for (int i = 0; i < 2; ++i) { int R, C; stage_rc(tid * 16 + i * 8192, R, C); const int Rb = Epi::PERM ? ((R & ~31) + perm32(R & 31)) : R;
;         voffB[i] = (unsigned)(Rb * K + C) * 2u; }
;     const size_t kstep = (size_t)(BK * 2);
;     const size_t hstep = (size_t)HALF * K * 2;
;     const unsigned ldsw = (unsigned)wid * 1024u;
;     const int aoff = lds_byte(wr * 64 + fr, fq * 8), boff = lds_byte(wc * 32 + fr, fq * 8);
;     ...
;     Unit cur, nxt; int ui = 0;
;     if (!S.next(0, cur)) return;
;     f32x4 acc[2][2][4][2];
; #pragma unroll
;     for (int a = 0; a < 2; ++a)
; #pragma unroll
;         for (int b = 0; b < 2; ++b)
; #pragma unroll
;             for (int m = 0; m < 4; ++m)
; #pragma unroll
;                 for (int n = 0; n < 2; ++n) acc[a][b][m][n] = (f32x4){0.f, 0.f, 0.f, 0.f};
;     bf16x8 At[4][2], B0[2][2], B1[2][2];
;     unsigned voffA[2][2];
;     PG8_AOFF(cur);
;     const char* Ab = (const char*)Abase;
;     const char* cB = S.b_ptr(cur);
;     PG8_STAGE(PG8_SB(0, 0), cB, voffB); PG8_STAGE(PG8_SA(0, 0), Ab, voffA[0]); PG8_STAGE(PG8_SB(0, 1), cB + hstep, voffB); PG8_STAGE(PG8_SA(0, 1), Ab, voffA[1]);
;     if (wr == 1) PG8_BAR;
.LBB0_1465:
	v_ashrrev_i32_e32 v6, 31, v5
	v_lshrrev_b32_e32 v6, 26, v6
	v_lshlrev_b32_e32 v0, 4, v5
	v_add_u32_e32 v6, v5, v6
	v_bfe_i32 v5, v5, 27, 1
	v_lshrrev_b32_e32 v5, 22, v5
	v_add_u32_e32 v5, v0, v5
	v_and_b32_e32 v5, 0xfffffc00, v5
	v_sub_u32_e32 v5, v0, v5
	v_lshrrev_b32_e32 v7, 4, v5
	v_bitop3_b32 v5, v7, v5, 32 bitop3:0x6c
	v_ashrrev_i32_e32 v8, 31, v5
	v_ashrrev_i32_e32 v6, 6, v6
	v_lshrrev_b32_e32 v8, 26, v8
	v_lshlrev_b32_e32 v7, 3, v6
	v_add_u32_e32 v8, v5, v8
	v_and_b32_e32 v7, -16, v7
	v_ashrrev_i32_e32 v9, 6, v8
	v_and_b32_e32 v8, 0xc0, v8
	v_add_u32_e32 v7, v9, v7
	v_sub_u32_e32 v5, v5, v8
	v_lshlrev_b32_e32 v6, 5, v6
	v_ashrrev_i16_sdwa v5, v216, sext(v5) dst_sel:DWORD dst_unused:UNUSED_PAD src0_sel:DWORD src1_sel:BYTE_0
	v_lshlrev_b32_e32 v8, 1, v7
	v_lshrrev_b32_e32 v10, 2, v7
	v_and_b32_e32 v9, 3, v9
	s_mov_b32 s1, 0x3fffe0
	v_and_b32_e32 v6, 32, v6
	v_bfe_i32 v5, v5, 0, 16
	v_and_b32_e32 v8, 24, v8
	v_and_b32_e32 v10, 4, v10
	v_and_or_b32 v7, v7, s1, v9
	v_or3_b32 v7, v7, v10, v8
	v_add_lshl_u32 v5, v6, v5, 1
	v_add_u32_e32 v0, 0x2000, v0
	v_lshl_add_u32 v180, v7, 10, v5
	v_ashrrev_i32_e32 v5, 31, v0
	v_lshrrev_b32_e32 v5, 22, v5
	v_add_u32_e32 v5, v0, v5
	v_ashrrev_i32_e32 v5, 10, v5
	v_mul_i32_i24_e32 v6, 0x400, v5
	v_sub_u32_e32 v0, v0, v6
	v_lshrrev_b32_e32 v6, 4, v0
	v_bitop3_b32 v0, v6, v0, 32 bitop3:0x6c
	v_ashrrev_i32_e32 v7, 31, v0
	v_lshrrev_b32_e32 v7, 26, v7
	v_lshlrev_b32_e32 v6, 3, v5
	v_add_u32_e32 v7, v0, v7
	v_and_b32_e32 v6, -16, v6
	v_ashrrev_i32_e32 v8, 6, v7
	v_and_b32_e32 v7, 0xc0, v7
	v_add_u32_e32 v6, v8, v6
	v_sub_u32_e32 v0, v0, v7
	v_lshlrev_b32_e32 v5, 5, v5
	v_ashrrev_i16_sdwa v0, v216, sext(v0) dst_sel:DWORD dst_unused:UNUSED_PAD src0_sel:DWORD src1_sel:BYTE_0
	v_lshlrev_b32_e32 v7, 1, v6
	v_lshrrev_b32_e32 v9, 2, v6
	v_and_b32_e32 v8, 3, v8
	v_and_b32_e32 v5, 32, v5
	v_bfe_i32 v0, v0, 0, 16
	v_and_b32_e32 v7, 24, v7
	v_and_b32_e32 v9, 4, v9
	v_and_or_b32 v6, v6, s1, v8
	v_or3_b32 v6, v6, v9, v7
	v_add_lshl_u32 v0, v5, v0, 1
	v_lshl_add_u32 v182, v6, 10, v0
	v_mbcnt_lo_u32_b32 v0, -1, 0
	v_mbcnt_hi_u32_b32 v0, -1, v0
	v_readlane_b32 s0, v254, 49
	v_or_b32_e32 v0, s75, v0
	v_ashrrev_i32_e32 v6, 31, v0
	v_lshrrev_b32_e32 v6, 26, v6
	v_lshlrev_b32_e32 v5, 4, v0
	v_add_u32_e32 v6, v0, v6
	v_bfe_i32 v0, v0, 27, 1
	v_lshrrev_b32_e32 v0, 22, v0
	v_add_u32_e32 v0, v5, v0
	v_and_b32_e32 v0, 0xfffffc00, v0
	v_sub_u32_e32 v0, v5, v0
	v_lshrrev_b32_e32 v7, 4, v0
	v_bitop3_b32 v0, v7, v0, 32 bitop3:0x6c
	v_ashrrev_i32_e32 v8, 31, v0
	v_lshrrev_b32_e32 v8, 26, v8
	v_add_u32_e32 v8, v0, v8
	v_ashrrev_i32_e32 v6, 6, v6
	v_ashrrev_i32_e32 v9, 6, v8
	v_and_b32_e32 v8, 0xc0, v8
	v_lshlrev_b32_e32 v7, 3, v6
	v_sub_u32_e32 v0, v0, v8
	v_and_b32_e32 v7, -16, v7
	v_lshlrev_b32_e32 v6, 5, v6
	v_ashrrev_i16_sdwa v0, v216, sext(v0) dst_sel:DWORD dst_unused:UNUSED_PAD src0_sel:DWORD src1_sel:BYTE_0
	v_add_u32_e32 v7, v9, v7
	v_and_b32_e32 v6, 32, v6
	v_bfe_i32 v0, v0, 0, 16
	v_add_u32_e32 v8, 0x80, v227
	v_add_lshl_u32 v6, v6, v0, 1
	v_add_u32_e32 v0, v7, v227
	v_add_u32_e32 v7, v7, v8
	v_add_u32_e32 v5, 0x2000, v5
	v_lshl_add_u32 v0, v0, 10, v6
	v_lshl_add_u32 v184, v7, 10, v6
	v_ashrrev_i32_e32 v6, 31, v5
	v_lshrrev_b32_e32 v6, 22, v6
	v_add_u32_e32 v6, v5, v6
	v_ashrrev_i32_e32 v6, 10, v6
	v_mul_i32_i24_e32 v7, 0x400, v6
	s_lshl_b32 s0, s0, 24
	v_sub_u32_e32 v5, v5, v7
	s_add_u32 s36, s6, s0
	v_lshrrev_b32_e32 v7, 4, v5
	s_addc_u32 s37, s7, 0
	v_bitop3_b32 v5, v7, v5, 32 bitop3:0x6c
	s_add_u32 s10, s8, 0x4090000
	v_ashrrev_i32_e32 v9, 31, v5
	s_addc_u32 s11, s9, 0
	s_ashr_i32 s1, s35, 6
	v_lshrrev_b32_e32 v9, 26, v9
	s_ashr_i32 s17, s16, 31
	s_ashr_i32 s0, s35, 8
	s_lshl_b32 s38, s1, 10
	v_add_u32_e32 v9, v5, v9
	s_lshl_b64 s[2:3], s[16:17], 18
	v_ashrrev_i32_e32 v10, 6, v9
	v_and_b32_e32 v9, 0xc0, v9
	s_add_u32 s2, s36, s2
	v_lshlrev_b32_e32 v7, 3, v6
	v_sub_u32_e32 v5, v5, v9
	s_addc_u32 s3, s37, s3
	s_add_i32 s17, s38, 0
	v_and_b32_e32 v7, -16, v7
	v_lshlrev_b32_e32 v6, 5, v6
	v_ashrrev_i16_sdwa v5, v216, sext(v5) dst_sel:DWORD dst_unused:UNUSED_PAD src0_sel:DWORD src1_sel:BYTE_0
	v_lshl_add_u64 v[2:3], s[2:3], 0, v[2:3]
	s_add_i32 s39, s17, 0x10000
	v_add_u32_e32 v7, v10, v7
	v_and_b32_e32 v6, 32, v6
	v_bfe_i32 v5, v5, 0, 16
	v_readfirstlane_b32 s2, v2
	v_readfirstlane_b32 s3, v3
	s_mov_b32 m0, s39
	s_add_i32 s42, s17, 0x12000
	v_add_lshl_u32 v5, v6, v5, 1
	v_add_u32_e32 v6, v7, v227
	v_lshl_add_u32 v186, v6, 10, v5
	global_load_lds_dwordx4 v180, s[2:3]
	s_mov_b32 m0, s42
	v_add_u32_e32 v6, v7, v8
	global_load_lds_dwordx4 v182, s[2:3]
	s_mov_b32 m0, s17
	s_add_i32 s43, s17, 0x2000
	v_lshl_add_u32 v188, v6, 10, v5
	global_load_lds_dwordx4 v0, s[10:11]
	s_mov_b32 m0, s43
	v_lshl_add_u64 v[6:7], v[2:3], 0, s[68:69]
	global_load_lds_dwordx4 v186, s[10:11]
	s_add_i32 m0, s17, 0x14000
	v_readfirstlane_b32 s2, v6
	v_readfirstlane_b32 s3, v7
	s_add_i32 s46, s17, 0x4000
	s_add_i32 s47, s17, 0x6000
	s_nop 2
	global_load_lds_dwordx4 v180, s[2:3]
	s_add_i32 m0, s17, 0x16000
	s_setprio 1
	s_cmp_lg_u32 s0, 1
	global_load_lds_dwordx4 v182, s[2:3]
	s_mov_b32 m0, s46
	s_nop 0
	global_load_lds_dwordx4 v184, s[10:11]
	s_mov_b32 m0, s47
	s_nop 0
	global_load_lds_dwordx4 v188, s[10:11]
	s_cbranch_scc1 .LBB0_1467
	s_barrier
	s_setprio 0
